# cmp phase: pass-1 items stream only the K tile (V tile DMA skipped until pass 2)
# baseline (speedup 1.0000x reference)
; #define LAS __attribute__((address_space(3)))
; #define RING_BARRIER() do { asm volatile("s_waitcnt lgkmcnt(0)" ::: "memory"); __builtin_amdgcn_s_barrier(); asm volatile("" ::: "memory"); } while (0)
; __device__ __forceinline__ void ring8_dma(const Ring8Lane& R, const char* K8p, const char* Vp, LAS unsigned char* sb, int wave) {
;     __builtin_amdgcn_global_load_lds((const unsigned*)(K8p + R.so[0]), (LAS unsigned*)(sb + wave * 1024), 16, 0, 0);
;     __builtin_amdgcn_global_load_lds((const unsigned*)((wave == 0 ? K8p : Vp) + R.so[1]), (LAS unsigned*)(sb + (wave + 8) * 1024), 16, 0, 0);
;     __builtin_amdgcn_global_load_lds((const unsigned*)(Vp + R.so[2]), (LAS unsigned*)(sb + (wave + 16) * 1024), 16, 0, 0);
;     if (wave <= 2) __builtin_amdgcn_global_load_lds((const unsigned*)(Vp + R.so[3]), (LAS unsigned*)(sb + (wave + 24) * 1024), 16, 0, 0);
; }
; __device__ __forceinline__ void cmp_phase(Frame& F) {
;     ...
;         for (int i = 0; i < nit; ++i) { const int kt = i < nkt ? i : i - nkt;
;             asm volatile("s_waitcnt vmcnt(0)" ::: "memory"); RING_BARRIER();
;             if (i + 1 < nit) { const int kn = (i + 1 < nkt) ? i + 1 : i + 1 - nkt; ring8_dma(RL, Kb + (size_t)kn * 8192, Vb + (size_t)kn * 16384, F.lds + ((i + 1) & 1) * SLOT8, F.wave); }
.LBB0_1572:
	s_waitcnt vmcnt(0)
	s_add_i32 s36, s80, 1
	s_waitcnt lgkmcnt(0)
	s_barrier
	s_cmp_ge_u32 s36, s74
	s_cselect_b64 s[54:55], -1, 0
	s_and_b64 vcc, exec, s[54:55]
	s_cbranch_vccnz .LBB0_1575
	s_add_i32 s22, s76, s80
	s_cmp_lt_u32 s80, s60
	s_cselect_b32 s48, s36, s22
	s_lshl_b64 s[22:23], s[48:49], 13
	s_add_u32 s56, s24, s22
	s_addc_u32 s57, s25, s23
	s_lshl_b64 s[22:23], s[48:49], 14
	s_add_u32 s22, s52, s22
	s_addc_u32 s23, s53, s23
	s_bitcmp1_b32 s36, 0
	s_cselect_b32 s37, 0x6c00, 0
	s_add_i32 s37, s65, s37
	s_and_b64 s[82:83], exec, s[44:45]
	v_lshl_add_u64 v[80:81], s[56:57], 0, v[114:115]
	s_mov_b32 m0, s37
	s_cselect_b32 s57, s57, s23
	s_cselect_b32 s56, s56, s22
	global_load_lds_dwordx4 v[80:81], off
	s_cmp_lt_u32 s80, s60
	s_cbranch_scc0 .Lcmp_dma_full
	s_and_b64 vcc, exec, s[44:45]
	s_cbranch_vccz .LBB0_1575
	v_lshl_add_u64 v[80:81], s[56:57], 0, v[122:123]
	s_add_i32 m0, s37, 0x2000
	s_nop 0
	global_load_lds_dwordx4 v[80:81], off
	s_branch .LBB0_1575
.Lcmp_dma_full:
	v_lshl_add_u64 v[80:81], s[56:57], 0, v[122:123]
	s_add_i32 m0, s37, 0x2000
	s_and_b64 vcc, exec, s[18:19]
	global_load_lds_dwordx4 v[80:81], off
	v_lshl_add_u64 v[80:81], s[22:23], 0, v[120:121]
	s_add_i32 m0, s37, 0x4000
	s_nop 0
	global_load_lds_dwordx4 v[80:81], off
	s_cbranch_vccnz .LBB0_1575
	v_lshl_add_u64 v[80:81], s[22:23], 0, v[124:125]
	s_add_i32 m0, s37, 0x6000
	s_nop 0
	global_load_lds_dwordx4 v[80:81], off
